# stack11 = stack10 + output-projection K loop rewritten the same way (weight loads spread between MFMAs, re-requested two k-steps ahead, last trip peeled)
# speedup vs baseline: 1.0155x; 1.0039x over previous
; DEVINL unsigned pk2(float lo, float hi) { const f32x2 v = {lo, hi}; return __builtin_bit_cast(unsigned, __builtin_convertvector(v, bf16v2)); }
; DEVINL float bflo(unsigned u) { return __uint_as_float(u << 16); }
; DEVINL float bfhi(unsigned u) { return __uint_as_float(u & 0xffff0000u); }
; DEVINL void phase4(const Params& P, unsigned char* smem) {
;     ...
;             const bf16_t* src = ATT + (size_t)(m0 + row) * DM;
; #pragma unroll 8
;             for (int i = 0; i < 16; ++i) {
;                 const int c = (t & 7) + 8 * i;
;                 u32x4 v = *(const u32x4*)(src + c * 8);
;                 const float sc = (c < 64) ? rna : rsw;
;                 v.x = pk2(bflo(v.x) * sc, bfhi(v.x) * sc); v.y = pk2(bflo(v.y) * sc, bfhi(v.y) * sc);
;                 v.z = pk2(bflo(v.z) * sc, bfhi(v.z) * sc); v.w = pk2(bflo(v.w) * sc, bfhi(v.w) * sc);
;                 *(u32x4*)(smem + row * 2048 + ((c ^ (row & 15)) << 4)) = v;
;             }
.LBB0_583:
	s_waitcnt vmcnt(8)
	v_mov_b32_e32 v2, v130
	v_mov_b32_e32 v3, v131
	v_mov_b32_e32 v4, v132
	v_mov_b32_e32 v5, v133
	v_mov_b32_e32 v6, v134
	v_mov_b32_e32 v7, v135
	v_mov_b32_e32 v8, v136
	v_mov_b32_e32 v9, v137
	v_mov_b32_e32 v14, v138
	v_mov_b32_e32 v15, v139
	v_mov_b32_e32 v16, v140
	v_mov_b32_e32 v17, v141
	v_mov_b32_e32 v18, v142
	v_mov_b32_e32 v19, v143
	v_mov_b32_e32 v20, v144
	v_mov_b32_e32 v21, v145
	v_mov_b32_e32 v22, v146
	v_mov_b32_e32 v23, v147
	v_mov_b32_e32 v24, v148
	v_mov_b32_e32 v25, v149
	v_mov_b32_e32 v26, v150
	v_mov_b32_e32 v27, v151
	v_mov_b32_e32 v28, v152
	v_mov_b32_e32 v29, v153
	v_mov_b32_e32 v30, v154
	v_mov_b32_e32 v31, v155
	v_mov_b32_e32 v32, v156
	v_mov_b32_e32 v33, v157
	v_mov_b32_e32 v34, v158
	v_mov_b32_e32 v35, v159
	v_mov_b32_e32 v36, v160
	v_mov_b32_e32 v37, v161
	v_add_u32_e32 v39, s0, v218
	s_cmp_eq_u32 s0, 0
	v_xor_b32_e32 v40, v39, v220
	v_add_u32_e32 v41, 8, v39
	v_add_u32_e32 v42, 16, v39
	v_add_u32_e32 v43, 24, v39
	v_add_u32_e32 v44, 32, v39
	s_cselect_b64 vcc, -1, 0
	v_add_u32_e32 v45, 40, v39
	v_add_u32_e32 v46, 48, v39
	v_add_u32_e32 v39, 56, v39
	v_lshl_add_u32 v102, v40, 4, v219
	v_xor_b32_e32 v40, v41, v220
	v_xor_b32_e32 v41, v42, v220
	v_xor_b32_e32 v42, v43, v220
	v_xor_b32_e32 v43, v44, v220
	v_cndmask_b32_e32 v38, v13, v12, vcc
	v_xor_b32_e32 v44, v45, v220
	v_xor_b32_e32 v45, v46, v220
	v_xor_b32_e32 v39, v39, v220
	v_lshl_add_u32 v103, v40, 4, v219
	v_lshl_add_u32 v104, v41, 4, v219
	v_lshl_add_u32 v105, v42, 4, v219
	v_lshl_add_u32 v106, v43, 4, v219
	s_add_i32 s0, s0, 64
	v_lshl_add_u32 v107, v44, 4, v219
	v_lshl_add_u32 v108, v45, 4, v219
	v_lshl_add_u64 v[10:11], v[10:11], 0, s[58:59]
	s_cmpk_eq_i32 s0, 0x80
	v_lshl_add_u32 v109, v39, 4, v219
	v_lshlrev_b32_e32 v40, 16, v2
	v_and_b32_e32 v41, 0xffff0000, v2
	v_lshlrev_b32_e32 v2, 16, v3
	v_and_b32_e32 v3, 0xffff0000, v3
	v_lshlrev_b32_e32 v42, 16, v4
	v_and_b32_e32 v43, 0xffff0000, v4
	v_lshlrev_b32_e32 v4, 16, v5
	v_and_b32_e32 v5, 0xffff0000, v5
	v_lshlrev_b32_e32 v44, 16, v6
	v_and_b32_e32 v45, 0xffff0000, v6
	v_lshlrev_b32_e32 v6, 16, v7
	v_and_b32_e32 v7, 0xffff0000, v7
	v_lshlrev_b32_e32 v46, 16, v8
	v_and_b32_e32 v47, 0xffff0000, v8
	v_lshlrev_b32_e32 v8, 16, v9
	v_and_b32_e32 v9, 0xffff0000, v9
	v_lshlrev_b32_e32 v48, 16, v14
	v_and_b32_e32 v49, 0xffff0000, v14
	v_lshlrev_b32_e32 v14, 16, v15
	v_and_b32_e32 v15, 0xffff0000, v15
	v_lshlrev_b32_e32 v50, 16, v16
	v_and_b32_e32 v51, 0xffff0000, v16
	v_lshlrev_b32_e32 v16, 16, v17
	v_and_b32_e32 v17, 0xffff0000, v17
	v_lshlrev_b32_e32 v52, 16, v18
	v_and_b32_e32 v53, 0xffff0000, v18
	v_lshlrev_b32_e32 v18, 16, v19
	v_and_b32_e32 v19, 0xffff0000, v19
	v_lshlrev_b32_e32 v54, 16, v20
	v_and_b32_e32 v55, 0xffff0000, v20
	v_lshlrev_b32_e32 v20, 16, v21
	v_and_b32_e32 v21, 0xffff0000, v21
	v_lshlrev_b32_e32 v56, 16, v22
	v_and_b32_e32 v57, 0xffff0000, v22
	v_lshlrev_b32_e32 v22, 16, v23
	v_and_b32_e32 v23, 0xffff0000, v23
	v_lshlrev_b32_e32 v58, 16, v24
	v_and_b32_e32 v59, 0xffff0000, v24
	v_lshlrev_b32_e32 v24, 16, v25
	v_and_b32_e32 v25, 0xffff0000, v25
	v_lshlrev_b32_e32 v60, 16, v26
	v_and_b32_e32 v61, 0xffff0000, v26
	v_lshlrev_b32_e32 v26, 16, v27
	v_and_b32_e32 v27, 0xffff0000, v27
	v_lshlrev_b32_e32 v62, 16, v28
	v_and_b32_e32 v63, 0xffff0000, v28
	v_lshlrev_b32_e32 v28, 16, v29
	v_and_b32_e32 v29, 0xffff0000, v29
	v_lshlrev_b32_e32 v64, 16, v30
	v_and_b32_e32 v65, 0xffff0000, v30
	v_lshlrev_b32_e32 v30, 16, v31
	v_and_b32_e32 v31, 0xffff0000, v31
	v_lshlrev_b32_e32 v66, 16, v32
	v_and_b32_e32 v67, 0xffff0000, v32
	v_lshlrev_b32_e32 v32, 16, v33
	v_and_b32_e32 v33, 0xffff0000, v33
	v_lshlrev_b32_e32 v68, 16, v34
	v_and_b32_e32 v69, 0xffff0000, v34
	v_lshlrev_b32_e32 v34, 16, v35
	v_and_b32_e32 v35, 0xffff0000, v35
	v_lshlrev_b32_e32 v70, 16, v36
	v_and_b32_e32 v71, 0xffff0000, v36
	v_lshlrev_b32_e32 v36, 16, v37
	v_and_b32_e32 v37, 0xffff0000, v37
	v_pk_mul_f32 v[40:41], v[38:39], v[40:41] op_sel_hi:[0,1]
	v_pk_mul_f32 v[72:73], v[38:39], v[2:3] op_sel_hi:[0,1]
	v_pk_mul_f32 v[42:43], v[38:39], v[42:43] op_sel_hi:[0,1]
	v_pk_mul_f32 v[74:75], v[38:39], v[4:5] op_sel_hi:[0,1]
	v_pk_mul_f32 v[44:45], v[38:39], v[44:45] op_sel_hi:[0,1]
	v_pk_mul_f32 v[76:77], v[38:39], v[6:7] op_sel_hi:[0,1]
	v_pk_mul_f32 v[46:47], v[38:39], v[46:47] op_sel_hi:[0,1]
	v_pk_mul_f32 v[78:79], v[38:39], v[8:9] op_sel_hi:[0,1]
	v_pk_mul_f32 v[48:49], v[38:39], v[48:49] op_sel_hi:[0,1]
	v_pk_mul_f32 v[80:81], v[38:39], v[14:15] op_sel_hi:[0,1]
	v_pk_mul_f32 v[50:51], v[38:39], v[50:51] op_sel_hi:[0,1]
	v_pk_mul_f32 v[82:83], v[38:39], v[16:17] op_sel_hi:[0,1]
	v_pk_mul_f32 v[52:53], v[38:39], v[52:53] op_sel_hi:[0,1]
	v_pk_mul_f32 v[84:85], v[38:39], v[18:19] op_sel_hi:[0,1]
	v_pk_mul_f32 v[54:55], v[38:39], v[54:55] op_sel_hi:[0,1]
	v_pk_mul_f32 v[86:87], v[38:39], v[20:21] op_sel_hi:[0,1]
	v_pk_mul_f32 v[56:57], v[38:39], v[56:57] op_sel_hi:[0,1]
	v_pk_mul_f32 v[88:89], v[38:39], v[22:23] op_sel_hi:[0,1]
	v_pk_mul_f32 v[58:59], v[38:39], v[58:59] op_sel_hi:[0,1]
	v_pk_mul_f32 v[90:91], v[38:39], v[24:25] op_sel_hi:[0,1]
	v_pk_mul_f32 v[60:61], v[38:39], v[60:61] op_sel_hi:[0,1]
	v_pk_mul_f32 v[92:93], v[38:39], v[26:27] op_sel_hi:[0,1]
	v_pk_mul_f32 v[62:63], v[38:39], v[62:63] op_sel_hi:[0,1]
	v_pk_mul_f32 v[94:95], v[38:39], v[28:29] op_sel_hi:[0,1]
	v_pk_mul_f32 v[64:65], v[38:39], v[64:65] op_sel_hi:[0,1]
	v_pk_mul_f32 v[96:97], v[38:39], v[30:31] op_sel_hi:[0,1]
	v_pk_mul_f32 v[66:67], v[38:39], v[66:67] op_sel_hi:[0,1]
	v_pk_mul_f32 v[98:99], v[38:39], v[32:33] op_sel_hi:[0,1]
	v_pk_mul_f32 v[68:69], v[38:39], v[68:69] op_sel_hi:[0,1]
	v_pk_mul_f32 v[100:101], v[38:39], v[34:35] op_sel_hi:[0,1]
; DEVINL unsigned pk2(float lo, float hi) { const f32x2 v = {lo, hi}; return __builtin_bit_cast(unsigned, __builtin_convertvector(v, bf16v2)); }
; DEVINL float bflo(unsigned u) { return __uint_as_float(u << 16); }
; DEVINL float bfhi(unsigned u) { return __uint_as_float(u & 0xffff0000u); }
; DEVINL void phase4(const Params& P, unsigned char* smem) {
;     ...
;             const bf16_t* src = ATT + (size_t)(m0 + row) * DM;
; #pragma unroll 8
;             for (int i = 0; i < 16; ++i) {
;                 const int c = (t & 7) + 8 * i;
;                 u32x4 v = *(const u32x4*)(src + c * 8);
;                 const float sc = (c < 64) ? rna : rsw;
;                 v.x = pk2(bflo(v.x) * sc, bfhi(v.x) * sc); v.y = pk2(bflo(v.y) * sc, bfhi(v.y) * sc);
;                 v.z = pk2(bflo(v.z) * sc, bfhi(v.z) * sc); v.w = pk2(bflo(v.w) * sc, bfhi(v.w) * sc);
;                 *(u32x4*)(smem + row * 2048 + ((c ^ (row & 15)) << 4)) = v;
;             }
	v_pk_mul_f32 v[70:71], v[38:39], v[70:71] op_sel_hi:[0,1]
	v_pk_mul_f32 v[38:39], v[38:39], v[36:37] op_sel_hi:[0,1]
	v_cvt_pk_bf16_f32 v2, v40, v41
	v_cvt_pk_bf16_f32 v3, v72, v73
	v_cvt_pk_bf16_f32 v4, v42, v43
	v_cvt_pk_bf16_f32 v5, v74, v75
	v_cvt_pk_bf16_f32 v6, v44, v45
	v_cvt_pk_bf16_f32 v7, v76, v77
	v_cvt_pk_bf16_f32 v8, v46, v47
	v_cvt_pk_bf16_f32 v9, v78, v79
	v_cvt_pk_bf16_f32 v14, v48, v49
	v_cvt_pk_bf16_f32 v15, v80, v81
	v_cvt_pk_bf16_f32 v16, v50, v51
	v_cvt_pk_bf16_f32 v17, v82, v83
	v_cvt_pk_bf16_f32 v18, v52, v53
	v_cvt_pk_bf16_f32 v19, v84, v85
	v_cvt_pk_bf16_f32 v20, v54, v55
	v_cvt_pk_bf16_f32 v21, v86, v87
	v_cvt_pk_bf16_f32 v22, v56, v57
	v_cvt_pk_bf16_f32 v23, v88, v89
	v_cvt_pk_bf16_f32 v24, v58, v59
	v_cvt_pk_bf16_f32 v25, v90, v91
	v_cvt_pk_bf16_f32 v26, v60, v61
	v_cvt_pk_bf16_f32 v27, v92, v93
	v_cvt_pk_bf16_f32 v28, v62, v63
	v_cvt_pk_bf16_f32 v29, v94, v95
	v_cvt_pk_bf16_f32 v30, v64, v65
	v_cvt_pk_bf16_f32 v31, v96, v97
	v_cvt_pk_bf16_f32 v32, v66, v67
	v_cvt_pk_bf16_f32 v33, v98, v99
	v_cvt_pk_bf16_f32 v34, v68, v69
	v_cvt_pk_bf16_f32 v35, v100, v101
	v_cvt_pk_bf16_f32 v36, v70, v71
	v_cvt_pk_bf16_f32 v37, v38, v39
	ds_write_b128 v102, v[2:5]
	ds_write_b128 v103, v[6:9]
	ds_write_b128 v104, v[14:17]
	ds_write_b128 v105, v[18:21]
	ds_write_b128 v106, v[22:25]
	ds_write_b128 v107, v[26:29]
	ds_write_b128 v108, v[30:33]
	ds_write_b128 v109, v[34:37]
	s_waitcnt vmcnt(0)
	v_mov_b32_e32 v2, v162
	v_mov_b32_e32 v3, v163
	v_mov_b32_e32 v4, v164
	v_mov_b32_e32 v5, v165
	v_mov_b32_e32 v6, v166
	v_mov_b32_e32 v7, v167
	v_mov_b32_e32 v8, v168
	v_mov_b32_e32 v9, v169
	v_mov_b32_e32 v14, v170
	v_mov_b32_e32 v15, v171
	v_mov_b32_e32 v16, v172
	v_mov_b32_e32 v17, v173
	v_mov_b32_e32 v18, v174
	v_mov_b32_e32 v19, v175
	v_mov_b32_e32 v20, v176
	v_mov_b32_e32 v21, v177
	v_mov_b32_e32 v22, v196
	v_mov_b32_e32 v23, v197
	v_mov_b32_e32 v24, v198
	v_mov_b32_e32 v25, v199
	v_mov_b32_e32 v26, v200
	v_mov_b32_e32 v27, v201
	v_mov_b32_e32 v28, v202
	v_mov_b32_e32 v29, v203
	v_mov_b32_e32 v30, v204
	v_mov_b32_e32 v31, v205
	v_mov_b32_e32 v32, v206
	v_mov_b32_e32 v33, v207
	v_mov_b32_e32 v34, v208
	v_mov_b32_e32 v35, v209
	v_mov_b32_e32 v36, v210
	v_mov_b32_e32 v37, v211
	v_add_u32_e32 v39, s0, v218
	s_cmp_eq_u32 s0, 0
	v_xor_b32_e32 v40, v39, v220
	v_add_u32_e32 v41, 8, v39
	v_add_u32_e32 v42, 16, v39
	v_add_u32_e32 v43, 24, v39
	v_add_u32_e32 v44, 32, v39
	s_cselect_b64 vcc, -1, 0
	v_add_u32_e32 v45, 40, v39
	v_add_u32_e32 v46, 48, v39
	v_add_u32_e32 v39, 56, v39
	v_lshl_add_u32 v102, v40, 4, v219
	v_xor_b32_e32 v40, v41, v220
	v_xor_b32_e32 v41, v42, v220
	v_xor_b32_e32 v42, v43, v220
	v_xor_b32_e32 v43, v44, v220
	v_cndmask_b32_e32 v38, v13, v12, vcc
	v_xor_b32_e32 v44, v45, v220
	v_xor_b32_e32 v45, v46, v220
	v_xor_b32_e32 v39, v39, v220
	v_lshl_add_u32 v103, v40, 4, v219
	v_lshl_add_u32 v104, v41, 4, v219
	v_lshl_add_u32 v105, v42, 4, v219
	v_lshl_add_u32 v106, v43, 4, v219
	s_add_i32 s0, s0, 64
	v_lshl_add_u32 v107, v44, 4, v219
	v_lshl_add_u32 v108, v45, 4, v219
	v_lshl_add_u64 v[10:11], v[10:11], 0, s[58:59]
	s_cmpk_eq_i32 s0, 0x80
	v_lshl_add_u32 v109, v39, 4, v219
	v_lshlrev_b32_e32 v40, 16, v2
	v_and_b32_e32 v41, 0xffff0000, v2
	v_lshlrev_b32_e32 v2, 16, v3
	v_and_b32_e32 v3, 0xffff0000, v3
	v_lshlrev_b32_e32 v42, 16, v4
	v_and_b32_e32 v43, 0xffff0000, v4
	v_lshlrev_b32_e32 v4, 16, v5
	v_and_b32_e32 v5, 0xffff0000, v5
	v_lshlrev_b32_e32 v44, 16, v6
	v_and_b32_e32 v45, 0xffff0000, v6
	v_lshlrev_b32_e32 v6, 16, v7
	v_and_b32_e32 v7, 0xffff0000, v7
	v_lshlrev_b32_e32 v46, 16, v8
	v_and_b32_e32 v47, 0xffff0000, v8
	v_lshlrev_b32_e32 v8, 16, v9
	v_and_b32_e32 v9, 0xffff0000, v9
	v_lshlrev_b32_e32 v48, 16, v14
	v_and_b32_e32 v49, 0xffff0000, v14
	v_lshlrev_b32_e32 v14, 16, v15
	v_and_b32_e32 v15, 0xffff0000, v15
	v_lshlrev_b32_e32 v50, 16, v16
	v_and_b32_e32 v51, 0xffff0000, v16
	v_lshlrev_b32_e32 v16, 16, v17
	v_and_b32_e32 v17, 0xffff0000, v17
	v_lshlrev_b32_e32 v52, 16, v18
	v_and_b32_e32 v53, 0xffff0000, v18
	v_lshlrev_b32_e32 v18, 16, v19
	v_and_b32_e32 v19, 0xffff0000, v19
	v_lshlrev_b32_e32 v54, 16, v20
	v_and_b32_e32 v55, 0xffff0000, v20
	v_lshlrev_b32_e32 v20, 16, v21
	v_and_b32_e32 v21, 0xffff0000, v21
	v_lshlrev_b32_e32 v56, 16, v22
	v_and_b32_e32 v57, 0xffff0000, v22
	v_lshlrev_b32_e32 v22, 16, v23
	v_and_b32_e32 v23, 0xffff0000, v23
	v_lshlrev_b32_e32 v58, 16, v24
	v_and_b32_e32 v59, 0xffff0000, v24
	v_lshlrev_b32_e32 v24, 16, v25
	v_and_b32_e32 v25, 0xffff0000, v25
	v_lshlrev_b32_e32 v60, 16, v26
	v_and_b32_e32 v61, 0xffff0000, v26
	v_lshlrev_b32_e32 v26, 16, v27
	v_and_b32_e32 v27, 0xffff0000, v27
	v_lshlrev_b32_e32 v62, 16, v28
	v_and_b32_e32 v63, 0xffff0000, v28
	v_lshlrev_b32_e32 v28, 16, v29
	v_and_b32_e32 v29, 0xffff0000, v29
	v_lshlrev_b32_e32 v64, 16, v30
	v_and_b32_e32 v65, 0xffff0000, v30
	v_lshlrev_b32_e32 v30, 16, v31
	v_and_b32_e32 v31, 0xffff0000, v31
	v_lshlrev_b32_e32 v66, 16, v32
	v_and_b32_e32 v67, 0xffff0000, v32
	v_lshlrev_b32_e32 v32, 16, v33
	v_and_b32_e32 v33, 0xffff0000, v33
	v_lshlrev_b32_e32 v68, 16, v34
	v_and_b32_e32 v69, 0xffff0000, v34
	v_lshlrev_b32_e32 v34, 16, v35
	v_and_b32_e32 v35, 0xffff0000, v35
	v_lshlrev_b32_e32 v70, 16, v36
	v_and_b32_e32 v71, 0xffff0000, v36
	v_lshlrev_b32_e32 v36, 16, v37
	v_and_b32_e32 v37, 0xffff0000, v37
	v_pk_mul_f32 v[40:41], v[38:39], v[40:41] op_sel_hi:[0,1]
	v_pk_mul_f32 v[72:73], v[38:39], v[2:3] op_sel_hi:[0,1]
	v_pk_mul_f32 v[42:43], v[38:39], v[42:43] op_sel_hi:[0,1]
	v_pk_mul_f32 v[74:75], v[38:39], v[4:5] op_sel_hi:[0,1]
	v_pk_mul_f32 v[44:45], v[38:39], v[44:45] op_sel_hi:[0,1]
	v_pk_mul_f32 v[76:77], v[38:39], v[6:7] op_sel_hi:[0,1]
; DEVINL unsigned pk2(float lo, float hi) { const f32x2 v = {lo, hi}; return __builtin_bit_cast(unsigned, __builtin_convertvector(v, bf16v2)); }
; DEVINL float bflo(unsigned u) { return __uint_as_float(u << 16); }
; DEVINL float bfhi(unsigned u) { return __uint_as_float(u & 0xffff0000u); }
; DEVINL void phase4(const Params& P, unsigned char* smem) {
;     ...
;             for (int i = 0; i < 16; ++i) {
;                 const int c = (t & 7) + 8 * i;
;                 u32x4 v = *(const u32x4*)(src + c * 8);
;                 const float sc = (c < 64) ? rna : rsw;
;                 v.x = pk2(bflo(v.x) * sc, bfhi(v.x) * sc); v.y = pk2(bflo(v.y) * sc, bfhi(v.y) * sc);
;                 v.z = pk2(bflo(v.z) * sc, bfhi(v.z) * sc); v.w = pk2(bflo(v.w) * sc, bfhi(v.w) * sc);
;                 *(u32x4*)(smem + row * 2048 + ((c ^ (row & 15)) << 4)) = v;
;             }
;         }
;         __syncthreads();
;         f32x4 acc[8][4];
; #pragma unroll
;         for (int i = 0; i < 8; ++i)
; #pragma unroll
;             for (int mi = 0; mi < 4; ++mi) acc[i][mi] = (f32x4){0.f, 0.f, 0.f, 0.f};
;         if (!SKIPF(32)) {
	v_pk_mul_f32 v[46:47], v[38:39], v[46:47] op_sel_hi:[0,1]
	v_pk_mul_f32 v[78:79], v[38:39], v[8:9] op_sel_hi:[0,1]
	v_pk_mul_f32 v[48:49], v[38:39], v[48:49] op_sel_hi:[0,1]
	v_pk_mul_f32 v[80:81], v[38:39], v[14:15] op_sel_hi:[0,1]
	v_pk_mul_f32 v[50:51], v[38:39], v[50:51] op_sel_hi:[0,1]
	v_pk_mul_f32 v[82:83], v[38:39], v[16:17] op_sel_hi:[0,1]
	v_pk_mul_f32 v[52:53], v[38:39], v[52:53] op_sel_hi:[0,1]
	v_pk_mul_f32 v[84:85], v[38:39], v[18:19] op_sel_hi:[0,1]
	v_pk_mul_f32 v[54:55], v[38:39], v[54:55] op_sel_hi:[0,1]
	v_pk_mul_f32 v[86:87], v[38:39], v[20:21] op_sel_hi:[0,1]
	v_pk_mul_f32 v[56:57], v[38:39], v[56:57] op_sel_hi:[0,1]
	v_pk_mul_f32 v[88:89], v[38:39], v[22:23] op_sel_hi:[0,1]
	v_pk_mul_f32 v[58:59], v[38:39], v[58:59] op_sel_hi:[0,1]
	v_pk_mul_f32 v[90:91], v[38:39], v[24:25] op_sel_hi:[0,1]
	v_pk_mul_f32 v[60:61], v[38:39], v[60:61] op_sel_hi:[0,1]
	v_pk_mul_f32 v[92:93], v[38:39], v[26:27] op_sel_hi:[0,1]
	v_pk_mul_f32 v[62:63], v[38:39], v[62:63] op_sel_hi:[0,1]
	v_pk_mul_f32 v[94:95], v[38:39], v[28:29] op_sel_hi:[0,1]
	v_pk_mul_f32 v[64:65], v[38:39], v[64:65] op_sel_hi:[0,1]
	v_pk_mul_f32 v[96:97], v[38:39], v[30:31] op_sel_hi:[0,1]
	v_pk_mul_f32 v[66:67], v[38:39], v[66:67] op_sel_hi:[0,1]
	v_pk_mul_f32 v[98:99], v[38:39], v[32:33] op_sel_hi:[0,1]
	v_pk_mul_f32 v[68:69], v[38:39], v[68:69] op_sel_hi:[0,1]
	v_pk_mul_f32 v[100:101], v[38:39], v[34:35] op_sel_hi:[0,1]
	v_pk_mul_f32 v[70:71], v[38:39], v[70:71] op_sel_hi:[0,1]
	v_pk_mul_f32 v[38:39], v[38:39], v[36:37] op_sel_hi:[0,1]
	v_cvt_pk_bf16_f32 v2, v40, v41
	v_cvt_pk_bf16_f32 v3, v72, v73
	v_cvt_pk_bf16_f32 v4, v42, v43
	v_cvt_pk_bf16_f32 v5, v74, v75
	v_cvt_pk_bf16_f32 v6, v44, v45
	v_cvt_pk_bf16_f32 v7, v76, v77
	v_cvt_pk_bf16_f32 v8, v46, v47
	v_cvt_pk_bf16_f32 v9, v78, v79
	v_cvt_pk_bf16_f32 v14, v48, v49
	v_cvt_pk_bf16_f32 v15, v80, v81
	v_cvt_pk_bf16_f32 v16, v50, v51
	v_cvt_pk_bf16_f32 v17, v82, v83
	v_cvt_pk_bf16_f32 v18, v52, v53
	v_cvt_pk_bf16_f32 v19, v84, v85
	v_cvt_pk_bf16_f32 v20, v54, v55
	v_cvt_pk_bf16_f32 v21, v86, v87
	v_cvt_pk_bf16_f32 v22, v56, v57
	v_cvt_pk_bf16_f32 v23, v88, v89
	v_cvt_pk_bf16_f32 v24, v58, v59
	v_cvt_pk_bf16_f32 v25, v90, v91
	v_cvt_pk_bf16_f32 v26, v60, v61
	v_cvt_pk_bf16_f32 v27, v92, v93
	v_cvt_pk_bf16_f32 v28, v62, v63
	v_cvt_pk_bf16_f32 v29, v94, v95
	v_cvt_pk_bf16_f32 v30, v64, v65
	v_cvt_pk_bf16_f32 v31, v96, v97
	v_cvt_pk_bf16_f32 v32, v66, v67
	v_cvt_pk_bf16_f32 v33, v98, v99
	v_cvt_pk_bf16_f32 v34, v68, v69
	v_cvt_pk_bf16_f32 v35, v100, v101
	v_cvt_pk_bf16_f32 v36, v70, v71
	v_cvt_pk_bf16_f32 v37, v38, v39
	ds_write_b128 v102, v[2:5]
	ds_write_b128 v103, v[6:9]
	ds_write_b128 v104, v[14:17]
	ds_write_b128 v105, v[18:21]
	ds_write_b128 v106, v[22:25]
	ds_write_b128 v107, v[26:29]
	ds_write_b128 v108, v[30:33]
	ds_write_b128 v109, v[34:37]
	v_mov_b32_e32 v5, 0
	v_and_b32_e32 v238, 15, v190
	v_ashrrev_i32_e32 v204, 4, v190
	s_and_b64 vcc, exec, s[42:43]
	v_mov_b32_e32 v4, v5
	v_mov_b32_e32 v3, v5
	v_mov_b32_e32 v2, v5
	v_mov_b32_e32 v9, v5
	v_mov_b32_e32 v8, v5
	v_mov_b32_e32 v7, v5
	v_mov_b32_e32 v6, v5
	v_mov_b32_e32 v69, v5
	v_mov_b32_e32 v68, v5
	v_mov_b32_e32 v67, v5
	v_mov_b32_e32 v66, v5
	v_mov_b32_e32 v73, v5
	v_mov_b32_e32 v72, v5
	v_mov_b32_e32 v71, v5
	v_mov_b32_e32 v70, v5
	v_mov_b32_e32 v13, v5
	v_mov_b32_e32 v12, v5
	v_mov_b32_e32 v11, v5
	v_mov_b32_e32 v10, v5
	v_mov_b32_e32 v17, v5
	v_mov_b32_e32 v16, v5
	v_mov_b32_e32 v15, v5
	v_mov_b32_e32 v14, v5
	v_mov_b32_e32 v77, v5
	v_mov_b32_e32 v76, v5
	v_mov_b32_e32 v75, v5
	v_mov_b32_e32 v74, v5
	v_mov_b32_e32 v81, v5
	v_mov_b32_e32 v80, v5
	v_mov_b32_e32 v79, v5
	v_mov_b32_e32 v78, v5
	v_mov_b32_e32 v21, v5
	v_mov_b32_e32 v20, v5
	v_mov_b32_e32 v19, v5
	v_mov_b32_e32 v18, v5
	v_mov_b32_e32 v25, v5
	v_mov_b32_e32 v24, v5
	v_mov_b32_e32 v23, v5
	v_mov_b32_e32 v22, v5
	v_mov_b32_e32 v85, v5
	v_mov_b32_e32 v84, v5
	v_mov_b32_e32 v83, v5
	v_mov_b32_e32 v82, v5
	v_mov_b32_e32 v89, v5
	v_mov_b32_e32 v88, v5
	v_mov_b32_e32 v87, v5
	v_mov_b32_e32 v86, v5
	v_mov_b32_e32 v29, v5
	v_mov_b32_e32 v28, v5
	v_mov_b32_e32 v27, v5
	v_mov_b32_e32 v26, v5
	v_mov_b32_e32 v33, v5
	v_mov_b32_e32 v32, v5
	v_mov_b32_e32 v31, v5
	v_mov_b32_e32 v30, v5
	v_mov_b32_e32 v93, v5
	v_mov_b32_e32 v92, v5
	v_mov_b32_e32 v91, v5
	v_mov_b32_e32 v90, v5
	v_mov_b32_e32 v97, v5
	v_mov_b32_e32 v96, v5
	v_mov_b32_e32 v95, v5
	v_mov_b32_e32 v94, v5
	v_mov_b32_e32 v129, v5
	v_mov_b32_e32 v128, v5
	v_mov_b32_e32 v127, v5
	v_mov_b32_e32 v126, v5
	v_mov_b32_e32 v125, v5
	v_mov_b32_e32 v124, v5
	v_mov_b32_e32 v123, v5
	v_mov_b32_e32 v122, v5
	v_mov_b32_e32 v65, v5
	v_mov_b32_e32 v64, v5
	v_mov_b32_e32 v63, v5
	v_mov_b32_e32 v62, v5
	v_mov_b32_e32 v61, v5
	v_mov_b32_e32 v60, v5
	v_mov_b32_e32 v59, v5
	v_mov_b32_e32 v58, v5
	v_mov_b32_e32 v121, v5
	v_mov_b32_e32 v120, v5
	v_mov_b32_e32 v119, v5
	v_mov_b32_e32 v118, v5
	v_mov_b32_e32 v117, v5
	v_mov_b32_e32 v116, v5
	v_mov_b32_e32 v115, v5
	v_mov_b32_e32 v114, v5
	v_mov_b32_e32 v57, v5
	v_mov_b32_e32 v56, v5
	v_mov_b32_e32 v55, v5
	v_mov_b32_e32 v54, v5
	v_mov_b32_e32 v53, v5
	v_mov_b32_e32 v52, v5
	v_mov_b32_e32 v51, v5
	v_mov_b32_e32 v50, v5
	v_mov_b32_e32 v113, v5
	v_mov_b32_e32 v112, v5
	v_mov_b32_e32 v111, v5
	v_mov_b32_e32 v110, v5
	v_mov_b32_e32 v109, v5
	v_mov_b32_e32 v108, v5
	v_mov_b32_e32 v107, v5
	v_mov_b32_e32 v106, v5
	v_mov_b32_e32 v49, v5
	v_mov_b32_e32 v48, v5
	v_mov_b32_e32 v47, v5
	v_mov_b32_e32 v46, v5
	v_mov_b32_e32 v45, v5
	v_mov_b32_e32 v44, v5
	v_mov_b32_e32 v43, v5
	v_mov_b32_e32 v42, v5
	v_mov_b32_e32 v105, v5
	v_mov_b32_e32 v104, v5
	v_mov_b32_e32 v103, v5
	v_mov_b32_e32 v102, v5
	v_mov_b32_e32 v101, v5
	v_mov_b32_e32 v100, v5
	v_mov_b32_e32 v99, v5
	v_mov_b32_e32 v98, v5
	v_mov_b32_e32 v41, v5
	v_mov_b32_e32 v40, v5
	v_mov_b32_e32 v39, v5
	v_mov_b32_e32 v38, v5
	v_mov_b32_e32 v37, v5
	v_mov_b32_e32 v36, v5
	v_mov_b32_e32 v35, v5
	v_mov_b32_e32 v34, v5
	s_waitcnt lgkmcnt(0)
	s_barrier
; #define LOADB(dst, ks_) do { const unsigned char* ub_ = wb + (size_t)((ks_) * 144) * 1024; \
;         _Pragma("unroll") for (int j_ = 0; j_ < 8; ++j_) dst[j_] = *(const bf16x8*)(ub_ + j_ * 1024 + voff); } while (0)
; #define LOADA(fd, ks_) do { _Pragma("unroll") for (int mi_ = 0; mi_ < 4; ++mi_) fd[mi_] = AFRAG(mi_, ks_); } while (0)
; #define LOADB(dst, ks_) do { const unsigned char* ub_ = wb + (size_t)((ks_) * 64) * 1024; \
;         _Pragma("unroll") for (int j_ = 0; j_ < 8; ++j_) dst[j_] = *(const bf16x8*)(ub_ + j_ * 1024 + voff); } while (0)
; #define LOADA(fd, ks_) do { _Pragma("unroll") for (int mi_ = 0; mi_ < 4; ++mi_) fd[mi_] = AFRAG(mi_, ks_); } while (0)
; DEVINL void phase4(const Params& P, unsigned char* smem) {
;     ...
;             const unsigned char* wb = (const unsigned char*)(P.ws + WS_WOF) + (size_t)(8 * wv) * 1024;
;             unsigned voff = (unsigned)(lane * 16);
;             asm volatile("" : "+v"(voff));
;             const int aoff = lr * 2048;
;     ...
;             bf16x8 b0[8], b1[8];
;     ...
;             bf16x8 fa[4];
;             LOADB(b0, 0); LOADA(fa, 0);
	s_cbranch_vccz .LBB0_587
	v_lshlrev_b32_e32 v178, 4, v190
	global_load_dwordx4 v[130:133], v178, s[44:45]
	global_load_dwordx4 v[134:137], v178, s[44:45] offset:1024
	global_load_dwordx4 v[138:141], v178, s[44:45] offset:2048
	global_load_dwordx4 v[142:145], v178, s[44:45] offset:3072
	v_lshl_add_u64 v[192:193], s[44:45], 0, v[178:179]
	v_add_co_u32_e32 v2, vcc, 0x1000, v192
	v_lshl_add_u32 v191, v238, 11, 0
	s_nop 0
	v_addc_co_u32_e32 v3, vcc, 0, v193, vcc
	global_load_dwordx4 v[158:161], v[2:3], off
	global_load_dwordx4 v[154:157], v[2:3], off offset:1024
	global_load_dwordx4 v[150:153], v[2:3], off offset:2048
	global_load_dwordx4 v[146:149], v[2:3], off offset:3072
	v_xor_b32_e32 v2, v204, v238
	v_lshl_add_u32 v2, v2, 4, v191
	v_add_u32_e32 v3, 0x10000, v2
	ds_read_b128 v[174:177], v2
	ds_read_b128 v[170:173], v2 offset:32768
	v_add_u32_e32 v2, 0x18000, v2
	ds_read_b128 v[166:169], v3
	ds_read_b128 v[162:165], v2
	v_mov_b32_e32 v34, 0
	s_mov_b32 s0, 0
	v_add_u32_e32 v196, 4, v204
	v_lshl_add_u64 v[194:195], s[52:53], 0, v[178:179]
	v_mov_b32_e32 v35, v34
	v_mov_b32_e32 v36, v34
	v_mov_b32_e32 v37, v34
	v_mov_b32_e32 v38, v34
	v_mov_b32_e32 v39, v34
	v_mov_b32_e32 v40, v34
	v_mov_b32_e32 v41, v34
	v_mov_b32_e32 v98, v34
	v_mov_b32_e32 v99, v34
	v_mov_b32_e32 v100, v34
	v_mov_b32_e32 v101, v34
	v_mov_b32_e32 v102, v34
	v_mov_b32_e32 v103, v34
	v_mov_b32_e32 v104, v34
	v_mov_b32_e32 v105, v34
	v_mov_b32_e32 v42, v34
	v_mov_b32_e32 v43, v34
	v_mov_b32_e32 v44, v34
	v_mov_b32_e32 v45, v34
	v_mov_b32_e32 v46, v34
	v_mov_b32_e32 v47, v34
	v_mov_b32_e32 v48, v34
	v_mov_b32_e32 v49, v34
	v_mov_b32_e32 v106, v34
	v_mov_b32_e32 v107, v34
	v_mov_b32_e32 v108, v34
	v_mov_b32_e32 v109, v34
	v_mov_b32_e32 v110, v34
	v_mov_b32_e32 v111, v34
	v_mov_b32_e32 v112, v34
	v_mov_b32_e32 v113, v34
	v_mov_b32_e32 v50, v34
	v_mov_b32_e32 v51, v34
	v_mov_b32_e32 v52, v34
	v_mov_b32_e32 v53, v34
	v_mov_b32_e32 v54, v34
	v_mov_b32_e32 v55, v34
	v_mov_b32_e32 v56, v34
	v_mov_b32_e32 v57, v34
	v_mov_b32_e32 v114, v34
	v_mov_b32_e32 v115, v34
	v_mov_b32_e32 v116, v34
	v_mov_b32_e32 v117, v34
	v_mov_b32_e32 v118, v34
	v_mov_b32_e32 v119, v34
	v_mov_b32_e32 v120, v34
	v_mov_b32_e32 v121, v34
	v_mov_b32_e32 v58, v34
	v_mov_b32_e32 v59, v34
	v_mov_b32_e32 v60, v34
	v_mov_b32_e32 v61, v34
	v_mov_b32_e32 v62, v34
	v_mov_b32_e32 v63, v34
	v_mov_b32_e32 v64, v34
	v_mov_b32_e32 v65, v34
	v_mov_b32_e32 v122, v34
	v_mov_b32_e32 v123, v34
	v_mov_b32_e32 v124, v34
	v_mov_b32_e32 v125, v34
	v_mov_b32_e32 v126, v34
	v_mov_b32_e32 v127, v34
	v_mov_b32_e32 v128, v34
	v_mov_b32_e32 v129, v34
	v_mov_b32_e32 v94, v34
	v_mov_b32_e32 v95, v34
	v_mov_b32_e32 v96, v34
	v_mov_b32_e32 v97, v34
	v_mov_b32_e32 v90, v34
	v_mov_b32_e32 v91, v34
	v_mov_b32_e32 v92, v34
	v_mov_b32_e32 v93, v34
	v_mov_b32_e32 v30, v34
	v_mov_b32_e32 v31, v34
	v_mov_b32_e32 v32, v34
	v_mov_b32_e32 v33, v34
	v_mov_b32_e32 v26, v34
	v_mov_b32_e32 v27, v34
	v_mov_b32_e32 v28, v34
	v_mov_b32_e32 v29, v34
	v_mov_b32_e32 v86, v34
	v_mov_b32_e32 v87, v34
	v_mov_b32_e32 v88, v34
	v_mov_b32_e32 v89, v34
	v_mov_b32_e32 v82, v34
	v_mov_b32_e32 v83, v34
	v_mov_b32_e32 v84, v34
	v_mov_b32_e32 v85, v34
	v_mov_b32_e32 v22, v34
	v_mov_b32_e32 v23, v34
	v_mov_b32_e32 v24, v34
	v_mov_b32_e32 v25, v34
	v_mov_b32_e32 v18, v34
	v_mov_b32_e32 v19, v34
	v_mov_b32_e32 v20, v34
	v_mov_b32_e32 v21, v34
	v_mov_b32_e32 v78, v34
	v_mov_b32_e32 v79, v34
	v_mov_b32_e32 v80, v34
	v_mov_b32_e32 v81, v34
	v_mov_b32_e32 v74, v34
	v_mov_b32_e32 v75, v34
	v_mov_b32_e32 v76, v34
	v_mov_b32_e32 v77, v34
	v_mov_b32_e32 v14, v34
	v_mov_b32_e32 v15, v34
	v_mov_b32_e32 v16, v34
	v_mov_b32_e32 v17, v34
	v_mov_b32_e32 v10, v34
	v_mov_b32_e32 v11, v34
	v_mov_b32_e32 v12, v34
	v_mov_b32_e32 v13, v34
	v_mov_b32_e32 v70, v34
	v_mov_b32_e32 v71, v34
	v_mov_b32_e32 v72, v34
	v_mov_b32_e32 v73, v34
	v_mov_b32_e32 v66, v34
	v_mov_b32_e32 v67, v34
	v_mov_b32_e32 v68, v34
	v_mov_b32_e32 v69, v34
	v_mov_b32_e32 v6, v34
	v_mov_b32_e32 v7, v34
	v_mov_b32_e32 v8, v34
	v_mov_b32_e32 v9, v34
	v_mov_b32_e32 v2, v34
	v_mov_b32_e32 v3, v34
	v_mov_b32_e32 v4, v34
	v_mov_b32_e32 v5, v34
	s_mov_b64 s[8:9], 0x1000
	v_lshl_add_u64 v[194:195], v[194:195], 0, s[8:9]
	global_load_dwordx4 v[198:201], v[194:195], off offset:-4096
	global_load_dwordx4 v[206:209], v[194:195], off offset:-3072
	global_load_dwordx4 v[210:213], v[194:195], off offset:-2048
	global_load_dwordx4 v[240:243], v[194:195], off offset:-1024
	global_load_dwordx4 v[244:247], v[194:195], off
	global_load_dwordx4 v[248:251], v[194:195], off offset:1024
	global_load_dwordx4 v[226:229], v[194:195], off offset:2048
	global_load_dwordx4 v[230:233], v[194:195], off offset:3072
; #define LOADB(dst, ks_) do { const unsigned char* ub_ = wb + (size_t)((ks_) * 144) * 1024; \
;         _Pragma("unroll") for (int j_ = 0; j_ < 8; ++j_) dst[j_] = *(const bf16x8*)(ub_ + j_ * 1024 + voff); } while (0)
; #define LOADA(fd, ks_) do { _Pragma("unroll") for (int mi_ = 0; mi_ < 4; ++mi_) fd[mi_] = AFRAG(mi_, ks_); } while (0)
; #define MMA(src, fs, ksn_) do { _Pragma("unroll") for (int mi_ = 0; mi_ < 4; ++mi_) { \
;         _Pragma("unroll") for (int j_ = 0; j_ < 8; ++j_) acc[j_][mi_] = __builtin_amdgcn_mfma_f32_16x16x32_bf16(src[j_], fs[mi_], acc[j_][mi_], 0, 0, 0); \
;         fs[mi_] = AFRAG(mi_, (ksn_) < 32 ? (ksn_) : 31); } } while (0)
; #define LOADB(dst, ks_) do { const unsigned char* ub_ = wb + (size_t)((ks_) * 64) * 1024; \
;         _Pragma("unroll") for (int j_ = 0; j_ < 8; ++j_) dst[j_] = *(const bf16x8*)(ub_ + j_ * 1024 + voff); } while (0)
; #define LOADA(fd, ks_) do { _Pragma("unroll") for (int mi_ = 0; mi_ < 4; ++mi_) fd[mi_] = AFRAG(mi_, ks_); } while (0)
; #define MMA(src, fs, ksn_) do { _Pragma("unroll") for (int mi_ = 0; mi_ < 4; ++mi_) { \
;         _Pragma("unroll") for (int j_ = 0; j_ < 8; ++j_) acc[j_][mi_] = __builtin_amdgcn_mfma_f32_16x16x32_bf16(src[j_], fs[mi_], acc[j_][mi_], 0, 0, 0); \
;         fs[mi_] = AFRAG(mi_, (ksn_) < 32 ? (ksn_) : 31); } } while (0)
; DEVINL void phase4(const Params& P, unsigned char* smem) {
;     ...
;             bf16x8 fa[4];
;             LOADB(b0, 0); LOADA(fa, 0);
; #pragma unroll 1
;             for (int ks = 0; ks < 32; ks += 2) {
;                 LOADB(b1, ks + 1);
;                 __builtin_amdgcn_sched_barrier(0);
;                 MMA(b0, fa, ks + 1);
;                 __builtin_amdgcn_sched_barrier(0);
;                 LOADB(b0, ks + 2 < 32 ? ks + 2 : 31);
;                 __builtin_amdgcn_sched_barrier(0);
;                 MMA(b1, fa, ks + 2);
;                 __builtin_amdgcn_sched_barrier(0);
;             }
.LBB0_586:
	s_add_i32 s1, s0, 2
	s_lshl_b32 s24, s1, 16
	s_add_i32 s24, s24, 0x1000
	v_xor_b32_e32 v236, v196, v238
	v_lshl_add_u32 v236, v236, 4, v191
	v_add_u32_e32 v237, 0x10000, v236
	v_lshl_add_u64 v[234:235], v[192:193], 0, s[24:25]
	s_waitcnt vmcnt(15) lgkmcnt(3)
	v_mfma_f32_16x16x32_bf16 v[126:129], v[130:133], v[174:177], v[126:129]
	s_waitcnt lgkmcnt(2)
	v_mfma_f32_16x16x32_bf16 v[122:125], v[130:133], v[170:173], v[122:125]
	s_waitcnt vmcnt(14)
	v_mfma_f32_16x16x32_bf16 v[118:121], v[134:137], v[174:177], v[118:121]
	v_mfma_f32_16x16x32_bf16 v[114:117], v[134:137], v[170:173], v[114:117]
	s_waitcnt vmcnt(13)
	v_mfma_f32_16x16x32_bf16 v[110:113], v[138:141], v[174:177], v[110:113]
	v_mfma_f32_16x16x32_bf16 v[106:109], v[138:141], v[170:173], v[106:109]
	s_waitcnt vmcnt(12)
	v_mfma_f32_16x16x32_bf16 v[102:105], v[142:145], v[174:177], v[102:105]
	v_mfma_f32_16x16x32_bf16 v[98:101], v[142:145], v[170:173], v[98:101]
	s_waitcnt vmcnt(11)
	v_mfma_f32_16x16x32_bf16 v[94:97], v[158:161], v[174:177], v[94:97]
	v_mfma_f32_16x16x32_bf16 v[90:93], v[158:161], v[170:173], v[90:93]
	s_waitcnt vmcnt(10)
	v_mfma_f32_16x16x32_bf16 v[86:89], v[154:157], v[174:177], v[86:89]
	v_mfma_f32_16x16x32_bf16 v[82:85], v[154:157], v[170:173], v[82:85]
	s_waitcnt vmcnt(9)
	v_mfma_f32_16x16x32_bf16 v[78:81], v[150:153], v[174:177], v[78:81]
	v_mfma_f32_16x16x32_bf16 v[74:77], v[150:153], v[170:173], v[74:77]
	s_waitcnt vmcnt(8)
	v_mfma_f32_16x16x32_bf16 v[70:73], v[146:149], v[174:177], v[70:73]
	v_mfma_f32_16x16x32_bf16 v[66:69], v[146:149], v[170:173], v[66:69]
	s_waitcnt lgkmcnt(1)
	v_mfma_f32_16x16x32_bf16 v[62:65], v[130:133], v[166:169], v[62:65]
	s_waitcnt lgkmcnt(0)
	v_mfma_f32_16x16x32_bf16 v[58:61], v[130:133], v[162:165], v[58:61]
	global_load_dwordx4 v[130:133], v[234:235], off offset:-4096
	v_mfma_f32_16x16x32_bf16 v[54:57], v[134:137], v[166:169], v[54:57]
	v_mfma_f32_16x16x32_bf16 v[50:53], v[134:137], v[162:165], v[50:53]
	global_load_dwordx4 v[134:137], v[234:235], off offset:-3072
	ds_read_b128 v[174:177], v236
	v_mfma_f32_16x16x32_bf16 v[46:49], v[138:141], v[166:169], v[46:49]
	v_mfma_f32_16x16x32_bf16 v[42:45], v[138:141], v[162:165], v[42:45]
	global_load_dwordx4 v[138:141], v[234:235], off offset:-2048
	ds_read_b128 v[170:173], v236 offset:32768
	v_mfma_f32_16x16x32_bf16 v[38:41], v[142:145], v[166:169], v[38:41]
	v_mfma_f32_16x16x32_bf16 v[34:37], v[142:145], v[162:165], v[34:37]
	global_load_dwordx4 v[142:145], v[234:235], off offset:-1024
	v_mfma_f32_16x16x32_bf16 v[30:33], v[158:161], v[166:169], v[30:33]
	v_mfma_f32_16x16x32_bf16 v[26:29], v[158:161], v[162:165], v[26:29]
	global_load_dwordx4 v[158:161], v[234:235], off
	v_mfma_f32_16x16x32_bf16 v[22:25], v[154:157], v[166:169], v[22:25]
	v_mfma_f32_16x16x32_bf16 v[18:21], v[154:157], v[162:165], v[18:21]
	global_load_dwordx4 v[154:157], v[234:235], off offset:1024
	v_mfma_f32_16x16x32_bf16 v[14:17], v[150:153], v[166:169], v[14:17]
	v_mfma_f32_16x16x32_bf16 v[10:13], v[150:153], v[162:165], v[10:13]
	global_load_dwordx4 v[150:153], v[234:235], off offset:2048
	v_mfma_f32_16x16x32_bf16 v[6:9], v[146:149], v[166:169], v[6:9]
	v_mfma_f32_16x16x32_bf16 v[2:5], v[146:149], v[162:165], v[2:5]
	global_load_dwordx4 v[146:149], v[234:235], off offset:3072
	ds_read_b128 v[166:169], v237
	ds_read_b128 v[162:165], v237 offset:32768
	v_lshl_add_u32 v236, s1, 2, v204
	v_lshl_add_u64 v[194:195], v[194:195], 0, s[60:61]
	v_xor_b32_e32 v236, v236, v238
	v_lshl_add_u32 v236, v236, 4, v191
	v_add_u32_e32 v237, 0x10000, v236
	s_waitcnt vmcnt(15) lgkmcnt(3)
	v_mfma_f32_16x16x32_bf16 v[126:129], v[198:201], v[174:177], v[126:129]
	s_waitcnt lgkmcnt(2)
	v_mfma_f32_16x16x32_bf16 v[122:125], v[198:201], v[170:173], v[122:125]
	s_waitcnt vmcnt(14)
	v_mfma_f32_16x16x32_bf16 v[118:121], v[206:209], v[174:177], v[118:121]
	v_mfma_f32_16x16x32_bf16 v[114:117], v[206:209], v[170:173], v[114:117]
	s_waitcnt vmcnt(13)
	v_mfma_f32_16x16x32_bf16 v[110:113], v[210:213], v[174:177], v[110:113]
	v_mfma_f32_16x16x32_bf16 v[106:109], v[210:213], v[170:173], v[106:109]
	s_waitcnt vmcnt(12)
	v_mfma_f32_16x16x32_bf16 v[102:105], v[240:243], v[174:177], v[102:105]
	v_mfma_f32_16x16x32_bf16 v[98:101], v[240:243], v[170:173], v[98:101]
	s_waitcnt vmcnt(11)
	v_mfma_f32_16x16x32_bf16 v[94:97], v[244:247], v[174:177], v[94:97]
	v_mfma_f32_16x16x32_bf16 v[90:93], v[244:247], v[170:173], v[90:93]
	s_waitcnt vmcnt(10)
	v_mfma_f32_16x16x32_bf16 v[86:89], v[248:251], v[174:177], v[86:89]
	v_mfma_f32_16x16x32_bf16 v[82:85], v[248:251], v[170:173], v[82:85]
	s_waitcnt vmcnt(9)
	v_mfma_f32_16x16x32_bf16 v[78:81], v[226:229], v[174:177], v[78:81]
	v_mfma_f32_16x16x32_bf16 v[74:77], v[226:229], v[170:173], v[74:77]
	s_waitcnt vmcnt(8)
	v_mfma_f32_16x16x32_bf16 v[70:73], v[230:233], v[174:177], v[70:73]
	v_mfma_f32_16x16x32_bf16 v[66:69], v[230:233], v[170:173], v[66:69]
	s_waitcnt lgkmcnt(1)
	v_mfma_f32_16x16x32_bf16 v[62:65], v[198:201], v[166:169], v[62:65]
	s_waitcnt lgkmcnt(0)
	v_mfma_f32_16x16x32_bf16 v[58:61], v[198:201], v[162:165], v[58:61]
	global_load_dwordx4 v[198:201], v[194:195], off offset:-4096
	v_mfma_f32_16x16x32_bf16 v[54:57], v[206:209], v[166:169], v[54:57]
	v_mfma_f32_16x16x32_bf16 v[50:53], v[206:209], v[162:165], v[50:53]
	global_load_dwordx4 v[206:209], v[194:195], off offset:-3072
	ds_read_b128 v[174:177], v236
	v_mfma_f32_16x16x32_bf16 v[46:49], v[210:213], v[166:169], v[46:49]
	v_mfma_f32_16x16x32_bf16 v[42:45], v[210:213], v[162:165], v[42:45]
	global_load_dwordx4 v[210:213], v[194:195], off offset:-2048
	ds_read_b128 v[170:173], v236 offset:32768
	v_mfma_f32_16x16x32_bf16 v[38:41], v[240:243], v[166:169], v[38:41]
	v_mfma_f32_16x16x32_bf16 v[34:37], v[240:243], v[162:165], v[34:37]
	global_load_dwordx4 v[240:243], v[194:195], off offset:-1024
	v_mfma_f32_16x16x32_bf16 v[30:33], v[244:247], v[166:169], v[30:33]
	v_mfma_f32_16x16x32_bf16 v[26:29], v[244:247], v[162:165], v[26:29]
	global_load_dwordx4 v[244:247], v[194:195], off
	v_mfma_f32_16x16x32_bf16 v[22:25], v[248:251], v[166:169], v[22:25]
	v_mfma_f32_16x16x32_bf16 v[18:21], v[248:251], v[162:165], v[18:21]
	global_load_dwordx4 v[248:251], v[194:195], off offset:1024
	v_mfma_f32_16x16x32_bf16 v[14:17], v[226:229], v[166:169], v[14:17]
	v_mfma_f32_16x16x32_bf16 v[10:13], v[226:229], v[162:165], v[10:13]
	global_load_dwordx4 v[226:229], v[194:195], off offset:2048
	v_mfma_f32_16x16x32_bf16 v[6:9], v[230:233], v[166:169], v[6:9]
	v_mfma_f32_16x16x32_bf16 v[2:5], v[230:233], v[162:165], v[2:5]
	global_load_dwordx4 v[230:233], v[194:195], off offset:3072
	ds_read_b128 v[166:169], v237
	ds_read_b128 v[162:165], v237 offset:32768
	v_add_u32_e32 v196, 8, v196
	s_mov_b32 s0, s1
	s_cmp_lt_u32 s0, 30
	s_cbranch_scc1 .LBB0_586
; #define LOADB(dst, ks_) do { const unsigned char* ub_ = wb + (size_t)((ks_) * 144) * 1024; \
;         _Pragma("unroll") for (int j_ = 0; j_ < 8; ++j_) dst[j_] = *(const bf16x8*)(ub_ + j_ * 1024 + voff); } while (0)
; #define LOADA(fd, ks_) do { _Pragma("unroll") for (int mi_ = 0; mi_ < 4; ++mi_) fd[mi_] = AFRAG(mi_, ks_); } while (0)
; #define MMA(src, fs, ksn_) do { _Pragma("unroll") for (int mi_ = 0; mi_ < 4; ++mi_) { \
;         _Pragma("unroll") for (int j_ = 0; j_ < 8; ++j_) acc[j_][mi_] = __builtin_amdgcn_mfma_f32_16x16x32_bf16(src[j_], fs[mi_], acc[j_][mi_], 0, 0, 0); \
;         fs[mi_] = AFRAG(mi_, (ksn_) < 32 ? (ksn_) : 31); } } while (0)
; #define LOADB(dst, ks_) do { const unsigned char* ub_ = wb + (size_t)((ks_) * 64) * 1024; \
;         _Pragma("unroll") for (int j_ = 0; j_ < 8; ++j_) dst[j_] = *(const bf16x8*)(ub_ + j_ * 1024 + voff); } while (0)
; #define LOADA(fd, ks_) do { _Pragma("unroll") for (int mi_ = 0; mi_ < 4; ++mi_) fd[mi_] = AFRAG(mi_, ks_); } while (0)
; #define MMA(src, fs, ksn_) do { _Pragma("unroll") for (int mi_ = 0; mi_ < 4; ++mi_) { \
;         _Pragma("unroll") for (int j_ = 0; j_ < 8; ++j_) acc[j_][mi_] = __builtin_amdgcn_mfma_f32_16x16x32_bf16(src[j_], fs[mi_], acc[j_][mi_], 0, 0, 0); \
;         fs[mi_] = AFRAG(mi_, (ksn_) < 32 ? (ksn_) : 31); } } while (0)
; DEVINL void phase4(const Params& P, unsigned char* smem) {
;     ...
;             bf16x8 fa[4];
;             LOADB(b0, 0); LOADA(fa, 0);
; #pragma unroll 1
;             for (int ks = 0; ks < 32; ks += 2) {
;                 LOADB(b1, ks + 1);
;                 __builtin_amdgcn_sched_barrier(0);
;                 MMA(b0, fa, ks + 1);
;                 __builtin_amdgcn_sched_barrier(0);
;                 LOADB(b0, ks + 2 < 32 ? ks + 2 : 31);
;                 __builtin_amdgcn_sched_barrier(0);
;                 MMA(b1, fa, ks + 2);
;                 __builtin_amdgcn_sched_barrier(0);
;             }
	v_xor_b32_e32 v236, v196, v238
	v_lshl_add_u32 v236, v236, 4, v191
	v_add_u32_e32 v237, 0x10000, v236
	s_waitcnt vmcnt(15) lgkmcnt(3)
	v_mfma_f32_16x16x32_bf16 v[126:129], v[130:133], v[174:177], v[126:129]
	s_waitcnt lgkmcnt(2)
	v_mfma_f32_16x16x32_bf16 v[122:125], v[130:133], v[170:173], v[122:125]
	s_waitcnt vmcnt(14)
	v_mfma_f32_16x16x32_bf16 v[118:121], v[134:137], v[174:177], v[118:121]
	v_mfma_f32_16x16x32_bf16 v[114:117], v[134:137], v[170:173], v[114:117]
	s_waitcnt vmcnt(13)
	v_mfma_f32_16x16x32_bf16 v[110:113], v[138:141], v[174:177], v[110:113]
	v_mfma_f32_16x16x32_bf16 v[106:109], v[138:141], v[170:173], v[106:109]
	s_waitcnt vmcnt(12)
	v_mfma_f32_16x16x32_bf16 v[102:105], v[142:145], v[174:177], v[102:105]
	v_mfma_f32_16x16x32_bf16 v[98:101], v[142:145], v[170:173], v[98:101]
	s_waitcnt vmcnt(11)
	v_mfma_f32_16x16x32_bf16 v[94:97], v[158:161], v[174:177], v[94:97]
	v_mfma_f32_16x16x32_bf16 v[90:93], v[158:161], v[170:173], v[90:93]
	s_waitcnt vmcnt(10)
	v_mfma_f32_16x16x32_bf16 v[86:89], v[154:157], v[174:177], v[86:89]
	v_mfma_f32_16x16x32_bf16 v[82:85], v[154:157], v[170:173], v[82:85]
	s_waitcnt vmcnt(9)
	v_mfma_f32_16x16x32_bf16 v[78:81], v[150:153], v[174:177], v[78:81]
	v_mfma_f32_16x16x32_bf16 v[74:77], v[150:153], v[170:173], v[74:77]
	s_waitcnt vmcnt(8)
	v_mfma_f32_16x16x32_bf16 v[70:73], v[146:149], v[174:177], v[70:73]
	v_mfma_f32_16x16x32_bf16 v[66:69], v[146:149], v[170:173], v[66:69]
	s_waitcnt lgkmcnt(1)
	v_mfma_f32_16x16x32_bf16 v[62:65], v[130:133], v[166:169], v[62:65]
	s_waitcnt lgkmcnt(0)
	v_mfma_f32_16x16x32_bf16 v[58:61], v[130:133], v[162:165], v[58:61]
	v_mfma_f32_16x16x32_bf16 v[54:57], v[134:137], v[166:169], v[54:57]
	v_mfma_f32_16x16x32_bf16 v[50:53], v[134:137], v[162:165], v[50:53]
	ds_read_b128 v[174:177], v236
	v_mfma_f32_16x16x32_bf16 v[46:49], v[138:141], v[166:169], v[46:49]
	v_mfma_f32_16x16x32_bf16 v[42:45], v[138:141], v[162:165], v[42:45]
	ds_read_b128 v[170:173], v236 offset:32768
	v_mfma_f32_16x16x32_bf16 v[38:41], v[142:145], v[166:169], v[38:41]
	v_mfma_f32_16x16x32_bf16 v[34:37], v[142:145], v[162:165], v[34:37]
	v_mfma_f32_16x16x32_bf16 v[30:33], v[158:161], v[166:169], v[30:33]
	v_mfma_f32_16x16x32_bf16 v[26:29], v[158:161], v[162:165], v[26:29]
	v_mfma_f32_16x16x32_bf16 v[22:25], v[154:157], v[166:169], v[22:25]
	v_mfma_f32_16x16x32_bf16 v[18:21], v[154:157], v[162:165], v[18:21]
	v_mfma_f32_16x16x32_bf16 v[14:17], v[150:153], v[166:169], v[14:17]
	v_mfma_f32_16x16x32_bf16 v[10:13], v[150:153], v[162:165], v[10:13]
	v_mfma_f32_16x16x32_bf16 v[6:9], v[146:149], v[166:169], v[6:9]
	v_mfma_f32_16x16x32_bf16 v[2:5], v[146:149], v[162:165], v[2:5]
	ds_read_b128 v[166:169], v237
	ds_read_b128 v[162:165], v237 offset:32768
	s_waitcnt vmcnt(7) lgkmcnt(3)
	v_mfma_f32_16x16x32_bf16 v[126:129], v[198:201], v[174:177], v[126:129]
	s_waitcnt lgkmcnt(2)
	v_mfma_f32_16x16x32_bf16 v[122:125], v[198:201], v[170:173], v[122:125]
	s_waitcnt vmcnt(6)
	v_mfma_f32_16x16x32_bf16 v[118:121], v[206:209], v[174:177], v[118:121]
	v_mfma_f32_16x16x32_bf16 v[114:117], v[206:209], v[170:173], v[114:117]
	s_waitcnt vmcnt(5)
	v_mfma_f32_16x16x32_bf16 v[110:113], v[210:213], v[174:177], v[110:113]
	v_mfma_f32_16x16x32_bf16 v[106:109], v[210:213], v[170:173], v[106:109]
	s_waitcnt vmcnt(4)
	v_mfma_f32_16x16x32_bf16 v[102:105], v[240:243], v[174:177], v[102:105]
	v_mfma_f32_16x16x32_bf16 v[98:101], v[240:243], v[170:173], v[98:101]
	s_waitcnt vmcnt(3)
	v_mfma_f32_16x16x32_bf16 v[94:97], v[244:247], v[174:177], v[94:97]
	v_mfma_f32_16x16x32_bf16 v[90:93], v[244:247], v[170:173], v[90:93]
	s_waitcnt vmcnt(2)
	v_mfma_f32_16x16x32_bf16 v[86:89], v[248:251], v[174:177], v[86:89]
	v_mfma_f32_16x16x32_bf16 v[82:85], v[248:251], v[170:173], v[82:85]
	s_waitcnt vmcnt(1)
	v_mfma_f32_16x16x32_bf16 v[78:81], v[226:229], v[174:177], v[78:81]
	v_mfma_f32_16x16x32_bf16 v[74:77], v[226:229], v[170:173], v[74:77]
	s_waitcnt vmcnt(0)
	v_mfma_f32_16x16x32_bf16 v[70:73], v[230:233], v[174:177], v[70:73]
	v_mfma_f32_16x16x32_bf16 v[66:69], v[230:233], v[170:173], v[66:69]
	s_waitcnt lgkmcnt(1)
	v_mfma_f32_16x16x32_bf16 v[62:65], v[198:201], v[166:169], v[62:65]
	s_waitcnt lgkmcnt(0)
	v_mfma_f32_16x16x32_bf16 v[58:61], v[198:201], v[162:165], v[58:61]
	v_mfma_f32_16x16x32_bf16 v[54:57], v[206:209], v[166:169], v[54:57]
	v_mfma_f32_16x16x32_bf16 v[50:53], v[206:209], v[162:165], v[50:53]
	v_mfma_f32_16x16x32_bf16 v[46:49], v[210:213], v[166:169], v[46:49]
	v_mfma_f32_16x16x32_bf16 v[42:45], v[210:213], v[162:165], v[42:45]
	v_mfma_f32_16x16x32_bf16 v[38:41], v[240:243], v[166:169], v[38:41]
	v_mfma_f32_16x16x32_bf16 v[34:37], v[240:243], v[162:165], v[34:37]
	v_mfma_f32_16x16x32_bf16 v[30:33], v[244:247], v[166:169], v[30:33]
	v_mfma_f32_16x16x32_bf16 v[26:29], v[244:247], v[162:165], v[26:29]
	v_mfma_f32_16x16x32_bf16 v[22:25], v[248:251], v[166:169], v[22:25]
	v_mfma_f32_16x16x32_bf16 v[18:21], v[248:251], v[162:165], v[18:21]
	v_mfma_f32_16x16x32_bf16 v[14:17], v[226:229], v[166:169], v[14:17]
	v_mfma_f32_16x16x32_bf16 v[10:13], v[226:229], v[162:165], v[10:13]
	v_mfma_f32_16x16x32_bf16 v[6:9], v[230:233], v[166:169], v[6:9]
	v_mfma_f32_16x16x32_bf16 v[2:5], v[230:233], v[162:165], v[2:5]
